# P9: next unit's schedule-table LDS reads issued inside the epilogue (second unit-top entry), as already done for P10
# baseline (speedup 1.0000x reference)
.Lp9_top2:
	s_add_i32 s29, s6, 1
	s_cmpk_gt_u32 s6, 0xfe
	s_mov_b64 s[54:55], 0
	s_cbranch_scc1 .LBB0_875
	s_waitcnt lgkmcnt(0)
	v_cmp_gt_i32_e32 vcc, 0, v240
	v_readfirstlane_b32 s4, v240
	s_cbranch_vccnz .LBB0_875
	v_mov_b32_e32 v5, v241
	s_mul_i32 s0, s29, s33
	s_add_i32 s0, s0, s64
	s_mov_b32 s5, s48
	s_mov_b64 s[54:55], -1
	v_readfirstlane_b32 s7, v242
	s_sub_i32 s0, s0, s7
	s_ashr_i32 s7, s0, 31
	s_lshr_b32 s7, s7, 30
	s_add_i32 s7, s0, s7
	s_ashr_i32 s28, s7, 2
	s_and_b32 s7, s7, -4
	s_sub_i32 s38, s0, s7
	s_lshl_b32 s0, s28, 8
	s_mov_b32 s96, s4
	v_add_u32_e32 v217, s0, v243
	s_lshl_b64 s[0:1], s[4:5], 21
	s_add_u32 s5, s10, s0
	s_addc_u32 s7, s11, s1
	s_ashr_i32 s39, s38, 31
	s_lshl_b64 s[0:1], s[38:39], 19
	s_add_u32 s0, s5, s0
	s_addc_u32 s1, s7, s1
	s_branch .LBB0_875

.LBB0_901:
	s_add_i32 s98, s29, 1
	s_lshl_b32 s98, s98, 2
	s_add_i32 s98, s98, 0x21160
	v_mov_b32_e32 v240, s98
	ds_read_b32 v240, v240
	v_exp_f32_e32 v4, v162
	v_exp_f32_e32 v5, v158
	v_exp_f32_e32 v6, v163
	v_exp_f32_e32 v7, v159
	v_add_f32_e32 v4, 1.0, v4
	v_exp_f32_e32 v8, v164
	s_lshl_b32 s4, s92, 7
	v_rcp_f32_e32 v4, v4
	v_add_f32_e32 v5, 1.0, v5
	v_exp_f32_e32 v9, v160
	s_and_b32 s4, s4, 0x7f80
	v_rcp_f32_e32 v5, v5
	v_add_f32_e32 v6, 1.0, v6
	v_exp_f32_e32 v10, v165
	v_add_u32_e32 v2, v218, v183
	v_or_b32_e32 v3, s4, v212
	v_rcp_f32_e32 v6, v6
	v_add_f32_e32 v7, 1.0, v7
	v_exp_f32_e32 v11, v161
	v_lshl_add_u32 v2, v2, 9, v3
	v_mul_f32_e32 v3, v170, v162
	v_rcp_f32_e32 v7, v7
	v_add_f32_e32 v8, 1.0, v8
	v_mul_f32_e32 v3, v3, v4
	v_mul_f32_e32 v4, v166, v158
	v_rcp_f32_e32 v8, v8
	v_add_f32_e32 v9, 1.0, v9
	v_mul_f32_e32 v5, v4, v5
	v_mul_f32_e32 v4, v171, v163
	v_rcp_f32_e32 v9, v9
	v_add_f32_e32 v10, 1.0, v10
	v_mul_f32_e32 v4, v4, v6
	v_mul_f32_e32 v6, v167, v159
	v_rcp_f32_e32 v10, v10
	v_add_f32_e32 v11, 1.0, v11
	v_mul_f32_e32 v6, v6, v7
	v_mul_f32_e32 v7, v172, v164
	v_rcp_f32_e32 v11, v11
	v_mul_f32_e32 v7, v7, v8
	v_mul_f32_e32 v8, v168, v160
	v_mul_f32_e32 v8, v8, v9
	v_mul_f32_e32 v9, v173, v165
	v_mul_f32_e32 v9, v9, v10
	v_mul_f32_e32 v10, v169, v161
	v_mul_f32_e32 v10, v10, v11
	v_med3_f32 v3, v3, s26, v216
	v_med3_f32 v11, v4, s26, v216
	v_mov_b32_e32 v4, v191
	v_cvt_pk_fp8_f32 v4, v3, v11
	v_med3_f32 v3, v5, s26, v216
	v_med3_f32 v6, v6, s26, v216
	v_mov_b32_e32 v5, v191
	v_cvt_pk_fp8_f32 v5, v3, v6
	v_med3_f32 v7, v7, s26, v216
	v_med3_f32 v9, v9, s26, v216
	v_cvt_pk_fp8_f32 v4, v7, v9 op_sel:[0,0,1]
	v_med3_f32 v7, v8, s26, v216
	v_med3_f32 v8, v10, s26, v216
	v_cvt_pk_fp8_f32 v5, v7, v8 op_sel:[0,0,1]
	s_nop 15
	s_nop 15
	v_exp_f32_e32 v6, v147
	v_exp_f32_e32 v7, v143
	global_store_dwordx2 v2, v[4:5], s[2:3]
	s_waitcnt lgkmcnt(0)
	v_readfirstlane_b32 s98, v240
	s_max_i32 s98, s98, 0
	s_lshl_b32 s98, s98, 2
	s_add_i32 s98, s98, 0x20200
	v_mov_b32_e32 v241, s98
	ds_read_b32 v242, v241
	ds_read_b32 v243, v241 offset:288
	ds_read_b32 v241, v241 offset:576
	v_exp_f32_e32 v4, v146
	v_exp_f32_e32 v5, v142
	v_exp_f32_e32 v8, v148
	v_exp_f32_e32 v9, v144
	v_add_f32_e32 v4, 1.0, v4
	v_rcp_f32_e32 v4, v4
	v_add_f32_e32 v5, 1.0, v5
	v_rcp_f32_e32 v5, v5
	v_add_f32_e32 v6, 1.0, v6
	v_exp_f32_e32 v10, v149
	v_rcp_f32_e32 v6, v6
	v_add_f32_e32 v7, 1.0, v7
	v_exp_f32_e32 v11, v145
	v_mul_f32_e32 v3, v154, v146
	v_rcp_f32_e32 v7, v7
	v_add_f32_e32 v8, 1.0, v8
	v_mul_f32_e32 v3, v3, v4
	v_mul_f32_e32 v4, v150, v142
	v_rcp_f32_e32 v8, v8
	v_add_f32_e32 v9, 1.0, v9
	v_mul_f32_e32 v5, v4, v5
	v_mul_f32_e32 v4, v155, v147
	v_rcp_f32_e32 v9, v9
	v_add_f32_e32 v10, 1.0, v10
	v_mul_f32_e32 v4, v4, v6
	v_mul_f32_e32 v6, v151, v143
	v_rcp_f32_e32 v10, v10
	v_add_f32_e32 v11, 1.0, v11
	v_mul_f32_e32 v6, v6, v7
	v_mul_f32_e32 v7, v156, v148
	v_rcp_f32_e32 v11, v11
	v_med3_f32 v3, v3, s26, v216
	v_med3_f32 v12, v4, s26, v216
	v_mov_b32_e32 v4, v191
	v_mul_f32_e32 v7, v7, v8
	v_mul_f32_e32 v8, v152, v144
	v_cvt_pk_fp8_f32 v4, v3, v12
	v_med3_f32 v3, v5, s26, v216
	v_med3_f32 v6, v6, s26, v216
	v_mov_b32_e32 v5, v191
	v_mul_f32_e32 v8, v8, v9
	v_mul_f32_e32 v9, v157, v149
	v_cvt_pk_fp8_f32 v5, v3, v6
	v_mul_f32_e32 v9, v9, v10
	v_mul_f32_e32 v10, v153, v145
	v_mul_f32_e32 v10, v10, v11
	v_med3_f32 v7, v7, s26, v216
	v_med3_f32 v9, v9, s26, v216
	v_cvt_pk_fp8_f32 v4, v7, v9 op_sel:[0,0,1]
	v_med3_f32 v7, v8, s26, v216
	v_med3_f32 v8, v10, s26, v216
	v_cvt_pk_fp8_f32 v5, v7, v8 op_sel:[0,0,1]
	v_add_u32_e32 v11, 0x2000, v2
	v_exp_f32_e32 v6, v131
	v_exp_f32_e32 v7, v127
	global_store_dwordx2 v11, v[4:5], s[2:3]
	v_exp_f32_e32 v4, v130
	v_exp_f32_e32 v5, v126
	v_exp_f32_e32 v8, v132
	v_exp_f32_e32 v9, v128
	v_add_f32_e32 v4, 1.0, v4
	v_rcp_f32_e32 v4, v4
	v_add_f32_e32 v5, 1.0, v5
	v_rcp_f32_e32 v5, v5
	v_add_f32_e32 v6, 1.0, v6
	v_exp_f32_e32 v10, v133
	v_rcp_f32_e32 v6, v6
	v_add_f32_e32 v7, 1.0, v7
	v_exp_f32_e32 v11, v129
	v_mul_f32_e32 v3, v138, v130
	v_rcp_f32_e32 v7, v7
	v_add_f32_e32 v8, 1.0, v8
	v_mul_f32_e32 v3, v3, v4
	v_mul_f32_e32 v4, v134, v126
	v_rcp_f32_e32 v8, v8
	v_add_f32_e32 v9, 1.0, v9
	v_mul_f32_e32 v5, v4, v5
	v_mul_f32_e32 v4, v139, v131
	v_rcp_f32_e32 v9, v9
	v_add_f32_e32 v10, 1.0, v10
	v_mul_f32_e32 v4, v4, v6
	v_mul_f32_e32 v6, v135, v127
	v_rcp_f32_e32 v10, v10
	v_add_f32_e32 v11, 1.0, v11
	v_mul_f32_e32 v6, v6, v7
	v_mul_f32_e32 v7, v140, v132
	v_rcp_f32_e32 v11, v11
	v_med3_f32 v3, v3, s26, v216
	v_med3_f32 v12, v4, s26, v216
	v_mov_b32_e32 v4, v191
	v_mul_f32_e32 v7, v7, v8
	v_mul_f32_e32 v8, v136, v128
	v_cvt_pk_fp8_f32 v4, v3, v12
	v_med3_f32 v3, v5, s26, v216
	v_med3_f32 v6, v6, s26, v216
	v_mov_b32_e32 v5, v191
	v_mul_f32_e32 v8, v8, v9
	v_mul_f32_e32 v9, v141, v133
	v_cvt_pk_fp8_f32 v5, v3, v6
	v_mul_f32_e32 v9, v9, v10
	v_mul_f32_e32 v10, v137, v129
	v_mul_f32_e32 v10, v10, v11
	v_med3_f32 v7, v7, s26, v216
	v_med3_f32 v9, v9, s26, v216
	v_cvt_pk_fp8_f32 v4, v7, v9 op_sel:[0,0,1]
	v_med3_f32 v7, v8, s26, v216
	v_med3_f32 v8, v10, s26, v216
	v_cvt_pk_fp8_f32 v5, v7, v8 op_sel:[0,0,1]
	v_add_u32_e32 v11, 0x4000, v2
	v_exp_f32_e32 v6, v111
	v_exp_f32_e32 v7, v107
	global_store_dwordx2 v11, v[4:5], s[2:3]
	v_exp_f32_e32 v4, v110
	v_exp_f32_e32 v5, v106
	v_exp_f32_e32 v8, v112
	v_exp_f32_e32 v9, v108
	v_add_f32_e32 v4, 1.0, v4
	v_rcp_f32_e32 v4, v4
	v_add_f32_e32 v5, 1.0, v5
	v_rcp_f32_e32 v5, v5
	v_add_f32_e32 v6, 1.0, v6
	v_exp_f32_e32 v10, v113
	v_rcp_f32_e32 v6, v6
	v_add_f32_e32 v7, 1.0, v7
	v_exp_f32_e32 v11, v109
	v_mul_f32_e32 v3, v122, v110
	v_rcp_f32_e32 v7, v7
	v_add_f32_e32 v8, 1.0, v8
	v_mul_f32_e32 v3, v3, v4
	v_mul_f32_e32 v4, v102, v106
	v_rcp_f32_e32 v8, v8
	v_add_f32_e32 v9, 1.0, v9
	v_mul_f32_e32 v5, v4, v5
	v_mul_f32_e32 v4, v123, v111
	v_rcp_f32_e32 v9, v9
	v_add_f32_e32 v10, 1.0, v10
	v_mul_f32_e32 v4, v4, v6
	v_mul_f32_e32 v6, v103, v107
	v_rcp_f32_e32 v10, v10
	v_add_f32_e32 v11, 1.0, v11
	v_mul_f32_e32 v6, v6, v7
	v_mul_f32_e32 v7, v124, v112
	v_rcp_f32_e32 v11, v11
	v_med3_f32 v3, v3, s26, v216
	v_med3_f32 v12, v4, s26, v216
	v_mov_b32_e32 v4, v191
	v_mul_f32_e32 v7, v7, v8
	v_mul_f32_e32 v8, v104, v108
	v_cvt_pk_fp8_f32 v4, v3, v12
	v_med3_f32 v3, v5, s26, v216
	v_med3_f32 v6, v6, s26, v216
	v_mov_b32_e32 v5, v191
	v_mul_f32_e32 v8, v8, v9
	v_mul_f32_e32 v9, v125, v113
	v_cvt_pk_fp8_f32 v5, v3, v6
	v_mul_f32_e32 v9, v9, v10
	v_mul_f32_e32 v10, v105, v109
	v_mul_f32_e32 v10, v10, v11
	v_med3_f32 v7, v7, s26, v216
	v_med3_f32 v9, v9, s26, v216
	v_cvt_pk_fp8_f32 v4, v7, v9 op_sel:[0,0,1]
	v_med3_f32 v7, v8, s26, v216
	v_med3_f32 v8, v10, s26, v216
	v_cvt_pk_fp8_f32 v5, v7, v8 op_sel:[0,0,1]
	v_add_u32_e32 v11, 0x6000, v2
	v_exp_f32_e32 v6, v94
	v_exp_f32_e32 v7, v99
	global_store_dwordx2 v11, v[4:5], s[2:3]
	v_exp_f32_e32 v5, v98
	v_exp_f32_e32 v8, v95
	v_exp_f32_e32 v9, v100
	v_add_f32_e32 v6, 1.0, v6
	v_add_f32_e32 v5, 1.0, v5
	v_rcp_f32_e32 v5, v5
	v_exp_f32_e32 v10, v96
	v_rcp_f32_e32 v6, v6
	v_add_f32_e32 v7, 1.0, v7
	v_exp_f32_e32 v11, v101
	v_rcp_f32_e32 v7, v7
	v_add_f32_e32 v8, 1.0, v8
	v_exp_f32_e32 v12, v97
	v_mul_f32_e32 v4, v118, v98
	v_rcp_f32_e32 v8, v8
	v_add_f32_e32 v9, 1.0, v9
	v_mul_f32_e32 v4, v4, v5
	v_mul_f32_e32 v5, v114, v94
	v_rcp_f32_e32 v9, v9
	v_add_f32_e32 v10, 1.0, v10
	v_mul_f32_e32 v5, v5, v6
	v_mul_f32_e32 v6, v119, v99
	v_rcp_f32_e32 v10, v10
	v_add_f32_e32 v11, 1.0, v11
	v_mul_f32_e32 v6, v6, v7
	v_mul_f32_e32 v7, v115, v95
	v_rcp_f32_e32 v11, v11
	v_add_f32_e32 v12, 1.0, v12
	v_mul_f32_e32 v7, v7, v8
	v_mul_f32_e32 v8, v120, v100
	v_rcp_f32_e32 v12, v12
	v_mul_f32_e32 v8, v8, v9
	v_mul_f32_e32 v9, v116, v96
	v_mul_f32_e32 v9, v9, v10
	v_mul_f32_e32 v10, v121, v101
	v_mul_f32_e32 v10, v10, v11
	v_mul_f32_e32 v11, v117, v97
	v_mul_f32_e32 v11, v11, v12
	v_med3_f32 v12, v4, s26, v216
	v_med3_f32 v6, v6, s26, v216
	v_mov_b32_e32 v4, v191
	v_cvt_pk_fp8_f32 v4, v12, v6
	v_med3_f32 v6, v5, s26, v216
	v_med3_f32 v7, v7, s26, v216
	v_mov_b32_e32 v5, v191
	v_cvt_pk_fp8_f32 v5, v6, v7
	v_med3_f32 v8, v8, s26, v216
	v_med3_f32 v10, v10, s26, v216
	v_cvt_pk_fp8_f32 v4, v8, v10 op_sel:[0,0,1]
	v_med3_f32 v8, v9, s26, v216
	v_med3_f32 v9, v11, s26, v216
	v_cvt_pk_fp8_f32 v5, v8, v9 op_sel:[0,0,1]
	v_add_u32_e32 v3, 0x10000, v2
	v_exp_f32_e32 v6, v91
	v_exp_f32_e32 v7, v87
	global_store_dwordx2 v3, v[4:5], s[2:3]
	v_exp_f32_e32 v4, v90
	v_exp_f32_e32 v5, v86
	v_exp_f32_e32 v8, v92
	v_exp_f32_e32 v9, v88
	v_add_f32_e32 v4, 1.0, v4
	v_rcp_f32_e32 v4, v4
	v_add_f32_e32 v5, 1.0, v5
	v_rcp_f32_e32 v5, v5
	v_add_f32_e32 v6, 1.0, v6
	v_exp_f32_e32 v10, v93
	v_rcp_f32_e32 v6, v6
	v_add_f32_e32 v7, 1.0, v7
	v_exp_f32_e32 v11, v89
	v_mul_f32_e32 v3, v62, v90
	v_rcp_f32_e32 v7, v7
	v_add_f32_e32 v8, 1.0, v8
	v_mul_f32_e32 v3, v3, v4
	v_mul_f32_e32 v4, v58, v86
	v_rcp_f32_e32 v8, v8
	v_add_f32_e32 v9, 1.0, v9
	v_mul_f32_e32 v5, v4, v5
	v_mul_f32_e32 v4, v63, v91
	v_rcp_f32_e32 v9, v9
	v_add_f32_e32 v10, 1.0, v10
	v_mul_f32_e32 v4, v4, v6
	v_mul_f32_e32 v6, v59, v87
	v_rcp_f32_e32 v10, v10
	v_add_f32_e32 v11, 1.0, v11
	v_mul_f32_e32 v6, v6, v7
	v_mul_f32_e32 v7, v64, v92
	v_rcp_f32_e32 v11, v11
	v_med3_f32 v3, v3, s26, v216
	v_med3_f32 v12, v4, s26, v216
	v_mov_b32_e32 v4, v191
	v_mul_f32_e32 v7, v7, v8
	v_mul_f32_e32 v8, v60, v88
	v_cvt_pk_fp8_f32 v4, v3, v12
	v_med3_f32 v3, v5, s26, v216
	v_med3_f32 v6, v6, s26, v216
	v_mov_b32_e32 v5, v191
	v_mul_f32_e32 v8, v8, v9
	v_mul_f32_e32 v9, v65, v93
	v_cvt_pk_fp8_f32 v5, v3, v6
	v_mul_f32_e32 v9, v9, v10
	v_mul_f32_e32 v10, v61, v89
	v_mul_f32_e32 v10, v10, v11
	v_med3_f32 v7, v7, s26, v216
	v_med3_f32 v9, v9, s26, v216
	v_cvt_pk_fp8_f32 v4, v7, v9 op_sel:[0,0,1]
	v_med3_f32 v7, v8, s26, v216
	v_med3_f32 v8, v10, s26, v216
	v_cvt_pk_fp8_f32 v5, v7, v8 op_sel:[0,0,1]
	v_add_u32_e32 v11, 0x12000, v2
	v_exp_f32_e32 v6, v83
	v_exp_f32_e32 v7, v79
	global_store_dwordx2 v11, v[4:5], s[2:3]
	v_exp_f32_e32 v4, v82
	v_exp_f32_e32 v5, v78
	v_exp_f32_e32 v8, v84
	v_exp_f32_e32 v9, v80
	v_add_f32_e32 v4, 1.0, v4
	v_rcp_f32_e32 v4, v4
	v_add_f32_e32 v5, 1.0, v5
	v_rcp_f32_e32 v5, v5
	v_add_f32_e32 v6, 1.0, v6
	v_exp_f32_e32 v10, v85
	v_rcp_f32_e32 v6, v6
	v_add_f32_e32 v7, 1.0, v7
	v_exp_f32_e32 v11, v81
	v_mul_f32_e32 v3, v54, v82
	v_rcp_f32_e32 v7, v7
	v_add_f32_e32 v8, 1.0, v8
	v_mul_f32_e32 v3, v3, v4
	v_mul_f32_e32 v4, v50, v78
	v_rcp_f32_e32 v8, v8
	v_add_f32_e32 v9, 1.0, v9
	v_mul_f32_e32 v5, v4, v5
	v_mul_f32_e32 v4, v55, v83
	v_rcp_f32_e32 v9, v9
	v_add_f32_e32 v10, 1.0, v10
	v_mul_f32_e32 v4, v4, v6
	v_mul_f32_e32 v6, v51, v79
	v_rcp_f32_e32 v10, v10
	v_add_f32_e32 v11, 1.0, v11
	v_mul_f32_e32 v6, v6, v7
	v_mul_f32_e32 v7, v56, v84
	v_rcp_f32_e32 v11, v11
	v_med3_f32 v3, v3, s26, v216
	v_med3_f32 v12, v4, s26, v216
	v_mov_b32_e32 v4, v191
	v_mul_f32_e32 v7, v7, v8
	v_mul_f32_e32 v8, v52, v80
	v_cvt_pk_fp8_f32 v4, v3, v12
	v_med3_f32 v3, v5, s26, v216
	v_med3_f32 v6, v6, s26, v216
	v_mov_b32_e32 v5, v191
	v_mul_f32_e32 v8, v8, v9
	v_mul_f32_e32 v9, v57, v85
	v_cvt_pk_fp8_f32 v5, v3, v6
	v_mul_f32_e32 v9, v9, v10
	v_mul_f32_e32 v10, v53, v81
	v_mul_f32_e32 v10, v10, v11
	v_med3_f32 v7, v7, s26, v216
	v_med3_f32 v9, v9, s26, v216
	v_cvt_pk_fp8_f32 v4, v7, v9 op_sel:[0,0,1]
	v_med3_f32 v7, v8, s26, v216
	v_med3_f32 v8, v10, s26, v216
	v_cvt_pk_fp8_f32 v5, v7, v8 op_sel:[0,0,1]
	v_add_u32_e32 v11, 0x14000, v2
	v_exp_f32_e32 v6, v75
	v_exp_f32_e32 v7, v71
	global_store_dwordx2 v11, v[4:5], s[2:3]
	v_exp_f32_e32 v4, v74
	v_exp_f32_e32 v5, v70
	v_exp_f32_e32 v8, v76
	v_exp_f32_e32 v9, v72
	v_add_f32_e32 v4, 1.0, v4
	v_rcp_f32_e32 v4, v4
	v_add_f32_e32 v5, 1.0, v5
	v_rcp_f32_e32 v5, v5
	v_add_f32_e32 v6, 1.0, v6
	v_exp_f32_e32 v10, v77
	v_rcp_f32_e32 v6, v6
	v_add_f32_e32 v7, 1.0, v7
	v_exp_f32_e32 v11, v73
	v_mul_f32_e32 v3, v42, v74
	v_rcp_f32_e32 v7, v7
	v_add_f32_e32 v8, 1.0, v8
	v_mul_f32_e32 v3, v3, v4
	v_mul_f32_e32 v4, v66, v70
	v_rcp_f32_e32 v8, v8
	v_add_f32_e32 v9, 1.0, v9
	v_mul_f32_e32 v4, v4, v5
	v_mul_f32_e32 v5, v43, v75
	v_rcp_f32_e32 v9, v9
	v_add_f32_e32 v10, 1.0, v10
	v_mul_f32_e32 v5, v5, v6
	v_mul_f32_e32 v6, v67, v71
	v_rcp_f32_e32 v10, v10
	v_add_f32_e32 v11, 1.0, v11
	v_mul_f32_e32 v6, v6, v7
	v_mul_f32_e32 v7, v44, v76
	v_rcp_f32_e32 v11, v11
	v_mul_f32_e32 v7, v7, v8
	v_mul_f32_e32 v8, v68, v72
	v_mul_f32_e32 v8, v8, v9
	v_mul_f32_e32 v9, v45, v77
	v_mul_f32_e32 v9, v9, v10
	v_mul_f32_e32 v10, v69, v73
	v_mul_f32_e32 v10, v10, v11
	v_add_u32_e32 v11, 0x16000, v2
	v_med3_f32 v3, v3, s26, v216
	v_med3_f32 v5, v5, s26, v216
	v_mov_b32_e32 v2, v191
	v_cvt_pk_fp8_f32 v2, v3, v5
	v_med3_f32 v4, v4, s26, v216
	v_med3_f32 v5, v6, s26, v216
	v_mov_b32_e32 v3, v191
	v_cvt_pk_fp8_f32 v3, v4, v5
	v_med3_f32 v7, v7, s26, v216
	v_med3_f32 v9, v9, s26, v216
	v_cvt_pk_fp8_f32 v2, v7, v9 op_sel:[0,0,1]
	v_med3_f32 v6, v8, s26, v216
	v_med3_f32 v7, v10, s26, v216
	v_cvt_pk_fp8_f32 v3, v6, v7 op_sel:[0,0,1]
	s_mov_b64 s[4:5], -1
	s_andn2_b64 vcc, exec, s[54:55]
	global_store_dwordx2 v11, v[2:3], s[2:3]
	s_cbranch_vccnz .LBB0_871
	s_andn2_b64 vcc, exec, s[80:81]
	s_cbranch_vccnz .LBB0_870
	s_barrier
	s_branch .LBB0_870
